# process_slot header and data LDS reads issued together (one wait) in the attention tile loops
# speedup vs baseline: 1.0047x; 1.0020x over previous
.LBB0_1594:
	s_andn2_b64 vcc, exec, s[8:9]
	s_cbranch_vccnz .LBB0_1598
	s_add_i32 s4, s19, -1
	s_lshr_b32 s4, s4, 1
	v_and_or_b32 v40, s4, 1, v232
	v_lshl_add_u32 v248, v40, 4, 0
	ds_read_b128 v[244:247], v248 offset:56320
	v_lshl_add_u32 v36, v40, 13, v233
	v_add_u32_e32 v48, 0xe000, v36
	ds_read2_b64 v[36:39], v48 offset1:16
	ds_read2_b64 v[40:43], v48 offset0:32 offset1:48
	ds_read2_b64 v[44:47], v48 offset0:64 offset1:80
	ds_read2_b64 v[48:51], v48 offset0:96 offset1:112
	s_waitcnt lgkmcnt(0)
	v_cmp_lt_i32_e32 vcc, -1, v244
	s_and_saveexec_b64 s[6:7], vcc
	s_cbranch_execz .LBB0_1597
	v_pk_mov_b32 v[56:57], v[244:245], v[246:247] op_sel:[1,0]
	v_cvt_pk_bf16_f32 v52, v36, v38
	v_cvt_pk_bf16_f32 v53, v40, v42
	v_cvt_pk_bf16_f32 v54, v44, v46
	v_cvt_pk_bf16_f32 v55, v48, v50
	v_cvt_pk_bf16_f32 v36, v37, v39
	v_cvt_pk_bf16_f32 v37, v41, v43
	v_lshl_add_u64 v[40:41], v[56:57], 0, v[200:201]
	v_cvt_pk_bf16_f32 v38, v45, v47
	v_cvt_pk_bf16_f32 v39, v49, v51
	global_store_dwordx4 v[40:41], v[52:55], off nt
	global_store_dwordx4 v[40:41], v[36:39], off offset:2048 nt

.LBB0_1617:
	s_lshr_b32 s4, s79, 1
	v_bitop3_b32 v56, s4, 1, v232 bitop3:0x26
	v_lshl_add_u32 v248, v56, 4, 0
	ds_read_b128 v[244:247], v248 offset:56320
	v_lshl_add_u32 v52, v56, 13, v233
	v_add_u32_e32 v84, 0xe000, v52
	ds_read2_b64 v[52:55], v84 offset1:16
	ds_read2_b64 v[56:59], v84 offset0:32 offset1:48
	ds_read2_b64 v[60:63], v84 offset0:64 offset1:80
	ds_read2_b64 v[84:87], v84 offset0:96 offset1:112
	s_waitcnt lgkmcnt(0)
	v_cmp_lt_i32_e32 vcc, -1, v244
	s_and_saveexec_b64 s[6:7], vcc
	s_cbranch_execz .LBB0_1619
	v_pk_mov_b32 v[92:93], v[244:245], v[246:247] op_sel:[1,0]
	v_cvt_pk_bf16_f32 v88, v52, v54
	v_cvt_pk_bf16_f32 v89, v56, v58
	v_cvt_pk_bf16_f32 v90, v60, v62
	v_cvt_pk_bf16_f32 v91, v84, v86
	v_cvt_pk_bf16_f32 v52, v53, v55
	v_cvt_pk_bf16_f32 v53, v57, v59
	v_lshl_add_u64 v[56:57], v[92:93], 0, v[200:201]
	v_cvt_pk_bf16_f32 v54, v61, v63
	v_cvt_pk_bf16_f32 v55, v85, v87
	global_store_dwordx4 v[56:57], v[88:91], off nt
	global_store_dwordx4 v[56:57], v[52:55], off offset:2048 nt

.LBB0_1999:
	s_andn2_b64 vcc, exec, s[48:49]
	s_cbranch_vccnz .LBB0_2003
	s_add_i32 s4, s12, -1
	s_lshr_b32 s4, s4, 1
	v_and_or_b32 v90, s4, 1, v149
	v_lshl_add_u32 v248, v90, 4, 0
	ds_read_b128 v[244:247], v248 offset:56320
	v_lshl_add_u32 v86, v90, 13, v198
	v_add_u32_e32 v98, 0xe000, v86
	ds_read2_b64 v[86:89], v98 offset1:16
	ds_read2_b64 v[90:93], v98 offset0:32 offset1:48
	ds_read2_b64 v[94:97], v98 offset0:64 offset1:80
	ds_read2_b64 v[100:103], v98 offset0:96 offset1:112
	s_waitcnt lgkmcnt(0)
	v_cmp_lt_i32_e32 vcc, -1, v244
	s_and_saveexec_b64 s[46:47], vcc
	s_cbranch_execz .LBB0_2002
	v_pk_mov_b32 v[108:109], v[244:245], v[246:247] op_sel:[1,0]
	v_cvt_pk_bf16_f32 v104, v86, v88
	v_cvt_pk_bf16_f32 v105, v90, v92
	v_cvt_pk_bf16_f32 v106, v94, v96
	v_cvt_pk_bf16_f32 v107, v100, v102
	v_cvt_pk_bf16_f32 v86, v87, v89
	v_cvt_pk_bf16_f32 v87, v91, v93
	v_lshl_add_u64 v[90:91], v[108:109], 0, v[156:157]
	v_cvt_pk_bf16_f32 v88, v95, v97
	v_cvt_pk_bf16_f32 v89, v101, v103
	global_store_dwordx4 v[90:91], v[104:107], off nt
	global_store_dwordx4 v[90:91], v[86:89], off offset:2048 nt

.LBB0_2027:
	s_lshr_b32 s4, s55, 1
	v_bitop3_b32 v54, s4, 1, v149 bitop3:0x26
	v_lshl_add_u32 v248, v54, 4, 0
	ds_read_b128 v[244:247], v248 offset:56320
	v_lshl_add_u32 v50, v54, 13, v198
	v_add_u32_e32 v62, 0xe000, v50
	ds_read2_b64 v[50:53], v62 offset1:16
	ds_read2_b64 v[54:57], v62 offset0:32 offset1:48
	ds_read2_b64 v[58:61], v62 offset0:64 offset1:80
	ds_read2_b64 v[62:65], v62 offset0:96 offset1:112
	s_waitcnt lgkmcnt(0)
	v_cmp_lt_i32_e32 vcc, -1, v244
	s_and_saveexec_b64 s[38:39], vcc
	s_cbranch_execz .LBB0_2029
	v_pk_mov_b32 v[70:71], v[244:245], v[246:247] op_sel:[1,0]
	v_cvt_pk_bf16_f32 v66, v50, v52
	v_cvt_pk_bf16_f32 v67, v54, v56
	v_cvt_pk_bf16_f32 v68, v58, v60
	v_cvt_pk_bf16_f32 v69, v62, v64
	v_cvt_pk_bf16_f32 v50, v51, v53
	v_cvt_pk_bf16_f32 v51, v55, v57
	v_lshl_add_u64 v[54:55], v[70:71], 0, v[156:157]
	v_cvt_pk_bf16_f32 v52, v59, v61
	v_cvt_pk_bf16_f32 v53, v63, v65
	global_store_dwordx4 v[54:55], v[66:69], off nt
	global_store_dwordx4 v[54:55], v[50:53], off offset:2048 nt
